# v11 + MoE-up SwiGLU epilogue rewritten: (g*u)*rcp(fma(exp2(g*c),invS,invS)), no register shuffles, one address chain; same f32/fp8 kinds
# baseline (speedup 1.0000x reference)
; __device__ __forceinline__ float opaque_f(float x) { asm volatile("" : "+v"(x)); return x; }
; __device__ __forceinline__ float fast_sigmoid(float x) { return __builtin_amdgcn_rcpf(1.f + __builtin_amdgcn_exp2f(-LOG2E * x)); }
; __device__ __forceinline__ u32x4 pack8(const f32x4 a, const f32x4 b) { u32x4 w; w.x = cvt_pk_bf16(a[0], a[1]); w.y = cvt_pk_bf16(a[2], a[3]); w.z = cvt_pk_bf16(b[0], b[1]); w.w = cvt_pk_bf16(b[2], b[3]); return w; }
;     __device__ __forceinline__ void operator()(const f32x4 (&acc)[2][2][4][2], const Unit& u, int wr, int wc, int fr, int fq, const float* pre = nullptr) const {
;     ...
;             for (int m = 0; m < 4; ++m) { const int row = EPI_ROWS(ai, m); float rs, gw = 1.f;
;                 if (MOE) { rs = (MOE_FP8 ? opaque_f(1.f / W13_SCALE) : srs[row]); gw = (HAS_PRE ? pre[ai * 4 + m] : sgw[row]) * (MOE_FP8 ? G8_SCALE : 1.f); } else { rs = rstd_q(ssq, row, fq) * ascale; if (f8) gw = G8_SCALE; }
;                 rs8[ai][m] = rs; gw8[ai][m] = gw; }
; #pragma unroll
;         for (int ai = 0; ai < 2; ++ai)
; #pragma unroll
;             for (int m = 0; m < 4; ++m) { const int row = EPI_ROWS(ai, m); const float rs = rs8[ai][m], gw = gw8[ai][m];
;                 const float rs2 = rs * gw; f32x4 o[2];
; #pragma unroll
;                 for (int bj = 0; bj < 2; ++bj)
; #pragma unroll
;                     for (int e = 0; e < 4; ++e) { const float a = acc[ai][bj][m][0][e] * rs, b = acc[ai][bj][m][1][e] * rs2; o[bj][e] = a * fast_sigmoid(a) * b; }
;                 if ((MOE && MOE_FP8) || (!MOE && f8)) { u32x2 w; w.x = pk4_fp8(o[0][0], o[0][1], o[0][2], o[0][3]); w.y = pk4_fp8(o[1][0], o[1][1], o[1][2], o[1][3]);
;                     *(u32x2*)((unsigned char*)G + (size_t)row * DFF + u.pn * HALF + wc * 32 + 8 * fq) = w; }
;                 else *(u32x4*)(G + (size_t)row * DFF + u.pn * HALF + wc * 32 + 8 * fq) = pack8(o[0], o[1]); }
.LBB0_1368:
	s_lshl_b32 s6, s84, 8
	s_add_i32 s6, s6, s56
	s_movk_i32 s66, 0xe00
	s_and_b64 vcc, exec, s[2:3]
	v_lshlrev_b32_e32 v0, 3, v198
	v_add_u32_e32 v3, s6, v197
	v_mov_b64_e32 v[6:7], s[10:11]
	v_ashrrev_i32_e32 v1, 31, v0
	v_mul_f32_e32 v54, 0x3b000000, v209
	v_mul_f32_e32 v55, 0x3b000000, v208
	v_mul_f32_e32 v56, 0x3b000000, v207
	v_mul_f32_e32 v57, 0x3b000000, v205
	v_mul_f32_e32 v58, 0x3b000000, v204
	v_mul_f32_e32 v59, 0x3b000000, v203
	v_mul_f32_e32 v60, 0x3b000000, v202
	v_mul_f32_e32 v61, 0x3b000000, v206
	v_mad_i64_i32 v[4:5], s[20:21], v3, s66, v[6:7]
	s_lshl_b32 s6, s83, 7
	s_ashr_i32 s7, s6, 31
	v_rcp_f32_e32 v54, v54
	v_rcp_f32_e32 v55, v55
	v_rcp_f32_e32 v56, v56
	v_rcp_f32_e32 v57, v57
	v_rcp_f32_e32 v58, v58
	v_rcp_f32_e32 v59, v59
	v_rcp_f32_e32 v60, v60
	v_rcp_f32_e32 v61, v61
	v_lshl_add_u64 v[4:5], v[4:5], 0, s[6:7]
	v_lshl_add_u64 v[4:5], v[4:5], 0, s[14:15]
	v_lshl_add_u64 v[4:5], v[4:5], 0, v[0:1]
	v_mul_f32_e32 v38, 0xbcb8aa3b, v184
	v_mul_f32_e32 v39, 0xbcb8aa3b, v185
	v_mul_f32_e32 v40, 0xbcb8aa3b, v186
	v_mul_f32_e32 v41, 0xbcb8aa3b, v187
	v_mul_f32_e32 v42, 0xbcb8aa3b, v176
	v_mul_f32_e32 v43, 0xbcb8aa3b, v177
	v_mul_f32_e32 v44, 0xbcb8aa3b, v178
	v_mul_f32_e32 v45, 0xbcb8aa3b, v179
	v_exp_f32_e32 v38, v38
	v_exp_f32_e32 v39, v39
	v_exp_f32_e32 v40, v40
	v_exp_f32_e32 v41, v41
	v_exp_f32_e32 v42, v42
	v_exp_f32_e32 v43, v43
	v_exp_f32_e32 v44, v44
	v_exp_f32_e32 v45, v45
	v_mul_f32_e32 v46, v184, v188
	v_mul_f32_e32 v47, v185, v189
	v_mul_f32_e32 v48, v186, v190
	v_mul_f32_e32 v49, v187, v191
	v_mul_f32_e32 v50, v176, v180
	v_mul_f32_e32 v51, v177, v181
	v_mul_f32_e32 v52, v178, v182
	v_mul_f32_e32 v53, v179, v183
	v_fma_f32 v38, v38, v54, v54
	v_fma_f32 v39, v39, v54, v54
	v_fma_f32 v40, v40, v54, v54
	v_fma_f32 v41, v41, v54, v54
	v_fma_f32 v42, v42, v54, v54
	v_fma_f32 v43, v43, v54, v54
	v_fma_f32 v44, v44, v54, v54
	v_fma_f32 v45, v45, v54, v54
	v_rcp_f32_e32 v38, v38
	v_rcp_f32_e32 v39, v39
	v_rcp_f32_e32 v40, v40
	v_rcp_f32_e32 v41, v41
	v_rcp_f32_e32 v42, v42
	v_rcp_f32_e32 v43, v43
	v_rcp_f32_e32 v44, v44
	v_rcp_f32_e32 v45, v45
	v_mul_f32_e32 v46, v46, v38
	v_mul_f32_e32 v47, v47, v39
	v_mul_f32_e32 v48, v48, v40
	v_mul_f32_e32 v49, v49, v41
	v_mul_f32_e32 v50, v50, v42
	v_mul_f32_e32 v51, v51, v43
	v_mul_f32_e32 v52, v52, v44
	v_mul_f32_e32 v53, v53, v45
	v_med3_f32 v46, v46, s49, v254
	v_med3_f32 v47, v47, s49, v254
	v_med3_f32 v48, v48, s49, v254
	v_med3_f32 v49, v49, s49, v254
	v_med3_f32 v50, v50, s49, v254
	v_med3_f32 v51, v51, s49, v254
	v_med3_f32 v52, v52, s49, v254
	v_med3_f32 v53, v53, s49, v254
	v_cvt_pk_fp8_f32 v32, v46, v47
	v_cvt_pk_fp8_f32 v33, v50, v51
	v_cvt_pk_fp8_f32 v32, v48, v49 op_sel:[0,0,1]
	v_cvt_pk_fp8_f32 v33, v52, v53 op_sel:[0,0,1]
	s_nop 0
	global_store_dwordx2 v[4:5], v[32:33], off
	s_mov_b32 s20, 0xe000
	s_mov_b32 s21, 0
	v_mul_f32_e32 v38, 0xbcb8aa3b, v168
	v_mul_f32_e32 v39, 0xbcb8aa3b, v169
	v_mul_f32_e32 v40, 0xbcb8aa3b, v170
	v_mul_f32_e32 v41, 0xbcb8aa3b, v171
	v_mul_f32_e32 v42, 0xbcb8aa3b, v160
	v_mul_f32_e32 v43, 0xbcb8aa3b, v161
	v_mul_f32_e32 v44, 0xbcb8aa3b, v162
	v_mul_f32_e32 v45, 0xbcb8aa3b, v163
	v_exp_f32_e32 v38, v38
	v_exp_f32_e32 v39, v39
	v_exp_f32_e32 v40, v40
	v_exp_f32_e32 v41, v41
	v_exp_f32_e32 v42, v42
	v_exp_f32_e32 v43, v43
	v_exp_f32_e32 v44, v44
	v_exp_f32_e32 v45, v45
	v_mul_f32_e32 v46, v168, v172
	v_mul_f32_e32 v47, v169, v173
	v_mul_f32_e32 v48, v170, v174
	v_mul_f32_e32 v49, v171, v175
	v_mul_f32_e32 v50, v160, v164
	v_mul_f32_e32 v51, v161, v165
	v_mul_f32_e32 v52, v162, v166
	v_mul_f32_e32 v53, v163, v167
	v_fma_f32 v38, v38, v55, v55
	v_fma_f32 v39, v39, v55, v55
	v_fma_f32 v40, v40, v55, v55
	v_fma_f32 v41, v41, v55, v55
	v_fma_f32 v42, v42, v55, v55
	v_fma_f32 v43, v43, v55, v55
	v_fma_f32 v44, v44, v55, v55
	v_fma_f32 v45, v45, v55, v55
	v_rcp_f32_e32 v38, v38
	v_rcp_f32_e32 v39, v39
	v_rcp_f32_e32 v40, v40
	v_rcp_f32_e32 v41, v41
	v_rcp_f32_e32 v42, v42
	v_rcp_f32_e32 v43, v43
	v_rcp_f32_e32 v44, v44
	v_rcp_f32_e32 v45, v45
	v_mul_f32_e32 v46, v46, v38
	v_mul_f32_e32 v47, v47, v39
	v_mul_f32_e32 v48, v48, v40
	v_mul_f32_e32 v49, v49, v41
	v_mul_f32_e32 v50, v50, v42
	v_mul_f32_e32 v51, v51, v43
	v_mul_f32_e32 v52, v52, v44
	v_mul_f32_e32 v53, v53, v45
	v_med3_f32 v46, v46, s49, v254
	v_med3_f32 v47, v47, s49, v254
	v_med3_f32 v48, v48, s49, v254
	v_med3_f32 v49, v49, s49, v254
	v_med3_f32 v50, v50, s49, v254
	v_med3_f32 v51, v51, s49, v254
	v_med3_f32 v52, v52, s49, v254
	v_med3_f32 v53, v53, s49, v254
	v_cvt_pk_fp8_f32 v34, v46, v47
	v_cvt_pk_fp8_f32 v35, v50, v51
	v_cvt_pk_fp8_f32 v34, v48, v49 op_sel:[0,0,1]
	v_cvt_pk_fp8_f32 v35, v52, v53 op_sel:[0,0,1]
	v_lshl_add_u64 v[8:9], v[4:5], 0, s[20:21]
	global_store_dwordx2 v[8:9], v[34:35], off
	s_mov_b32 s20, 0x1c000
	s_mov_b32 s21, 0
	v_mul_f32_e32 v38, 0xbcb8aa3b, v152
	v_mul_f32_e32 v39, 0xbcb8aa3b, v153
	v_mul_f32_e32 v40, 0xbcb8aa3b, v154
	v_mul_f32_e32 v41, 0xbcb8aa3b, v155
	v_mul_f32_e32 v42, 0xbcb8aa3b, v144
	v_mul_f32_e32 v43, 0xbcb8aa3b, v145
	v_mul_f32_e32 v44, 0xbcb8aa3b, v146
	v_mul_f32_e32 v45, 0xbcb8aa3b, v147
	v_exp_f32_e32 v38, v38
	v_exp_f32_e32 v39, v39
	v_exp_f32_e32 v40, v40
	v_exp_f32_e32 v41, v41
	v_exp_f32_e32 v42, v42
	v_exp_f32_e32 v43, v43
	v_exp_f32_e32 v44, v44
	v_exp_f32_e32 v45, v45
	v_mul_f32_e32 v46, v152, v156
	v_mul_f32_e32 v47, v153, v157
	v_mul_f32_e32 v48, v154, v158
	v_mul_f32_e32 v49, v155, v159
	v_mul_f32_e32 v50, v144, v148
	v_mul_f32_e32 v51, v145, v149
	v_mul_f32_e32 v52, v146, v150
	v_mul_f32_e32 v53, v147, v151
	v_fma_f32 v38, v38, v56, v56
	v_fma_f32 v39, v39, v56, v56
	v_fma_f32 v40, v40, v56, v56
	v_fma_f32 v41, v41, v56, v56
; __device__ __forceinline__ float opaque_f(float x) { asm volatile("" : "+v"(x)); return x; }
; __device__ __forceinline__ float fast_sigmoid(float x) { return __builtin_amdgcn_rcpf(1.f + __builtin_amdgcn_exp2f(-LOG2E * x)); }
; __device__ __forceinline__ u32x4 pack8(const f32x4 a, const f32x4 b) { u32x4 w; w.x = cvt_pk_bf16(a[0], a[1]); w.y = cvt_pk_bf16(a[2], a[3]); w.z = cvt_pk_bf16(b[0], b[1]); w.w = cvt_pk_bf16(b[2], b[3]); return w; }
;     __device__ __forceinline__ void operator()(const f32x4 (&acc)[2][2][4][2], const Unit& u, int wr, int wc, int fr, int fq, const float* pre = nullptr) const {
;     ...
;             for (int m = 0; m < 4; ++m) { const int row = EPI_ROWS(ai, m); float rs, gw = 1.f;
;                 if (MOE) { rs = (MOE_FP8 ? opaque_f(1.f / W13_SCALE) : srs[row]); gw = (HAS_PRE ? pre[ai * 4 + m] : sgw[row]) * (MOE_FP8 ? G8_SCALE : 1.f); } else { rs = rstd_q(ssq, row, fq) * ascale; if (f8) gw = G8_SCALE; }
;                 rs8[ai][m] = rs; gw8[ai][m] = gw; }
; #pragma unroll
;         for (int ai = 0; ai < 2; ++ai)
; #pragma unroll
;             for (int m = 0; m < 4; ++m) { const int row = EPI_ROWS(ai, m); const float rs = rs8[ai][m], gw = gw8[ai][m];
;                 const float rs2 = rs * gw; f32x4 o[2];
; #pragma unroll
;                 for (int bj = 0; bj < 2; ++bj)
; #pragma unroll
;                     for (int e = 0; e < 4; ++e) { const float a = acc[ai][bj][m][0][e] * rs, b = acc[ai][bj][m][1][e] * rs2; o[bj][e] = a * fast_sigmoid(a) * b; }
;                 if ((MOE && MOE_FP8) || (!MOE && f8)) { u32x2 w; w.x = pk4_fp8(o[0][0], o[0][1], o[0][2], o[0][3]); w.y = pk4_fp8(o[1][0], o[1][1], o[1][2], o[1][3]);
;                     *(u32x2*)((unsigned char*)G + (size_t)row * DFF + u.pn * HALF + wc * 32 + 8 * fq) = w; }
;                 else *(u32x4*)(G + (size_t)row * DFF + u.pn * HALF + wc * 32 + 8 * fq) = pack8(o[0], o[1]); }
	v_fma_f32 v42, v42, v56, v56
	v_fma_f32 v43, v43, v56, v56
	v_fma_f32 v44, v44, v56, v56
	v_fma_f32 v45, v45, v56, v56
	v_rcp_f32_e32 v38, v38
	v_rcp_f32_e32 v39, v39
	v_rcp_f32_e32 v40, v40
	v_rcp_f32_e32 v41, v41
	v_rcp_f32_e32 v42, v42
	v_rcp_f32_e32 v43, v43
	v_rcp_f32_e32 v44, v44
	v_rcp_f32_e32 v45, v45
	v_mul_f32_e32 v46, v46, v38
	v_mul_f32_e32 v47, v47, v39
	v_mul_f32_e32 v48, v48, v40
	v_mul_f32_e32 v49, v49, v41
	v_mul_f32_e32 v50, v50, v42
	v_mul_f32_e32 v51, v51, v43
	v_mul_f32_e32 v52, v52, v44
	v_mul_f32_e32 v53, v53, v45
	v_med3_f32 v46, v46, s49, v254
	v_med3_f32 v47, v47, s49, v254
	v_med3_f32 v48, v48, s49, v254
	v_med3_f32 v49, v49, s49, v254
	v_med3_f32 v50, v50, s49, v254
	v_med3_f32 v51, v51, s49, v254
	v_med3_f32 v52, v52, s49, v254
	v_med3_f32 v53, v53, s49, v254
	v_cvt_pk_fp8_f32 v32, v46, v47
	v_cvt_pk_fp8_f32 v33, v50, v51
	v_cvt_pk_fp8_f32 v32, v48, v49 op_sel:[0,0,1]
	v_cvt_pk_fp8_f32 v33, v52, v53 op_sel:[0,0,1]
	v_lshl_add_u64 v[8:9], v[4:5], 0, s[20:21]
	global_store_dwordx2 v[8:9], v[32:33], off
	s_mov_b32 s20, 0x2a000
	s_mov_b32 s21, 0
	v_mul_f32_e32 v38, 0xbcb8aa3b, v136
	v_mul_f32_e32 v39, 0xbcb8aa3b, v137
	v_mul_f32_e32 v40, 0xbcb8aa3b, v138
	v_mul_f32_e32 v41, 0xbcb8aa3b, v139
	v_mul_f32_e32 v42, 0xbcb8aa3b, v128
	v_mul_f32_e32 v43, 0xbcb8aa3b, v129
	v_mul_f32_e32 v44, 0xbcb8aa3b, v130
	v_mul_f32_e32 v45, 0xbcb8aa3b, v131
	v_exp_f32_e32 v38, v38
	v_exp_f32_e32 v39, v39
	v_exp_f32_e32 v40, v40
	v_exp_f32_e32 v41, v41
	v_exp_f32_e32 v42, v42
	v_exp_f32_e32 v43, v43
	v_exp_f32_e32 v44, v44
	v_exp_f32_e32 v45, v45
	v_mul_f32_e32 v46, v136, v140
	v_mul_f32_e32 v47, v137, v141
	v_mul_f32_e32 v48, v138, v142
	v_mul_f32_e32 v49, v139, v143
	v_mul_f32_e32 v50, v128, v132
	v_mul_f32_e32 v51, v129, v133
	v_mul_f32_e32 v52, v130, v134
	v_mul_f32_e32 v53, v131, v135
	v_fma_f32 v38, v38, v57, v57
	v_fma_f32 v39, v39, v57, v57
	v_fma_f32 v40, v40, v57, v57
	v_fma_f32 v41, v41, v57, v57
	v_fma_f32 v42, v42, v57, v57
	v_fma_f32 v43, v43, v57, v57
	v_fma_f32 v44, v44, v57, v57
	v_fma_f32 v45, v45, v57, v57
	v_rcp_f32_e32 v38, v38
	v_rcp_f32_e32 v39, v39
	v_rcp_f32_e32 v40, v40
	v_rcp_f32_e32 v41, v41
	v_rcp_f32_e32 v42, v42
	v_rcp_f32_e32 v43, v43
	v_rcp_f32_e32 v44, v44
	v_rcp_f32_e32 v45, v45
	v_mul_f32_e32 v46, v46, v38
	v_mul_f32_e32 v47, v47, v39
	v_mul_f32_e32 v48, v48, v40
	v_mul_f32_e32 v49, v49, v41
	v_mul_f32_e32 v50, v50, v42
	v_mul_f32_e32 v51, v51, v43
	v_mul_f32_e32 v52, v52, v44
	v_mul_f32_e32 v53, v53, v45
	v_med3_f32 v46, v46, s49, v254
	v_med3_f32 v47, v47, s49, v254
	v_med3_f32 v48, v48, s49, v254
	v_med3_f32 v49, v49, s49, v254
	v_med3_f32 v50, v50, s49, v254
	v_med3_f32 v51, v51, s49, v254
	v_med3_f32 v52, v52, s49, v254
	v_med3_f32 v53, v53, s49, v254
	v_cvt_pk_fp8_f32 v34, v46, v47
	v_cvt_pk_fp8_f32 v35, v50, v51
	v_cvt_pk_fp8_f32 v34, v48, v49 op_sel:[0,0,1]
	v_cvt_pk_fp8_f32 v35, v52, v53 op_sel:[0,0,1]
	v_lshl_add_u64 v[8:9], v[4:5], 0, s[20:21]
	global_store_dwordx2 v[8:9], v[34:35], off
	s_mov_b32 s20, 0x70000
	s_mov_b32 s21, 0
	v_mul_f32_e32 v38, 0xbcb8aa3b, v120
	v_mul_f32_e32 v39, 0xbcb8aa3b, v121
	v_mul_f32_e32 v40, 0xbcb8aa3b, v122
	v_mul_f32_e32 v41, 0xbcb8aa3b, v123
	v_mul_f32_e32 v42, 0xbcb8aa3b, v112
	v_mul_f32_e32 v43, 0xbcb8aa3b, v113
	v_mul_f32_e32 v44, 0xbcb8aa3b, v114
	v_mul_f32_e32 v45, 0xbcb8aa3b, v115
	v_exp_f32_e32 v38, v38
	v_exp_f32_e32 v39, v39
	v_exp_f32_e32 v40, v40
	v_exp_f32_e32 v41, v41
	v_exp_f32_e32 v42, v42
	v_exp_f32_e32 v43, v43
	v_exp_f32_e32 v44, v44
	v_exp_f32_e32 v45, v45
	v_mul_f32_e32 v46, v120, v124
	v_mul_f32_e32 v47, v121, v125
	v_mul_f32_e32 v48, v122, v126
	v_mul_f32_e32 v49, v123, v127
	v_mul_f32_e32 v50, v112, v116
	v_mul_f32_e32 v51, v113, v117
	v_mul_f32_e32 v52, v114, v118
	v_mul_f32_e32 v53, v115, v119
	v_fma_f32 v38, v38, v58, v58
	v_fma_f32 v39, v39, v58, v58
	v_fma_f32 v40, v40, v58, v58
	v_fma_f32 v41, v41, v58, v58
	v_fma_f32 v42, v42, v58, v58
	v_fma_f32 v43, v43, v58, v58
	v_fma_f32 v44, v44, v58, v58
	v_fma_f32 v45, v45, v58, v58
	v_rcp_f32_e32 v38, v38
	v_rcp_f32_e32 v39, v39
	v_rcp_f32_e32 v40, v40
	v_rcp_f32_e32 v41, v41
	v_rcp_f32_e32 v42, v42
	v_rcp_f32_e32 v43, v43
	v_rcp_f32_e32 v44, v44
	v_rcp_f32_e32 v45, v45
	v_mul_f32_e32 v46, v46, v38
	v_mul_f32_e32 v47, v47, v39
	v_mul_f32_e32 v48, v48, v40
	v_mul_f32_e32 v49, v49, v41
	v_mul_f32_e32 v50, v50, v42
	v_mul_f32_e32 v51, v51, v43
	v_mul_f32_e32 v52, v52, v44
	v_mul_f32_e32 v53, v53, v45
	v_med3_f32 v46, v46, s49, v254
	v_med3_f32 v47, v47, s49, v254
	v_med3_f32 v48, v48, s49, v254
	v_med3_f32 v49, v49, s49, v254
	v_med3_f32 v50, v50, s49, v254
	v_med3_f32 v51, v51, s49, v254
	v_med3_f32 v52, v52, s49, v254
	v_med3_f32 v53, v53, s49, v254
	v_cvt_pk_fp8_f32 v32, v46, v47
	v_cvt_pk_fp8_f32 v33, v50, v51
	v_cvt_pk_fp8_f32 v32, v48, v49 op_sel:[0,0,1]
	v_cvt_pk_fp8_f32 v33, v52, v53 op_sel:[0,0,1]
	v_lshl_add_u64 v[8:9], v[4:5], 0, s[20:21]
	global_store_dwordx2 v[8:9], v[32:33], off
	s_mov_b32 s20, 0x7e000
	s_mov_b32 s21, 0
	v_mul_f32_e32 v38, 0xbcb8aa3b, v104
	v_mul_f32_e32 v39, 0xbcb8aa3b, v105
	v_mul_f32_e32 v40, 0xbcb8aa3b, v106
	v_mul_f32_e32 v41, 0xbcb8aa3b, v107
	v_mul_f32_e32 v42, 0xbcb8aa3b, v96
	v_mul_f32_e32 v43, 0xbcb8aa3b, v97
	v_mul_f32_e32 v44, 0xbcb8aa3b, v98
	v_mul_f32_e32 v45, 0xbcb8aa3b, v99
	v_exp_f32_e32 v38, v38
	v_exp_f32_e32 v39, v39
	v_exp_f32_e32 v40, v40
	v_exp_f32_e32 v41, v41
	v_exp_f32_e32 v42, v42
	v_exp_f32_e32 v43, v43
	v_exp_f32_e32 v44, v44
; __device__ __forceinline__ float opaque_f(float x) { asm volatile("" : "+v"(x)); return x; }
; __device__ __forceinline__ float fast_sigmoid(float x) { return __builtin_amdgcn_rcpf(1.f + __builtin_amdgcn_exp2f(-LOG2E * x)); }
; __device__ __forceinline__ u32x4 pack8(const f32x4 a, const f32x4 b) { u32x4 w; w.x = cvt_pk_bf16(a[0], a[1]); w.y = cvt_pk_bf16(a[2], a[3]); w.z = cvt_pk_bf16(b[0], b[1]); w.w = cvt_pk_bf16(b[2], b[3]); return w; }
;     __device__ __forceinline__ void operator()(const f32x4 (&acc)[2][2][4][2], const Unit& u, int wr, int wc, int fr, int fq, const float* pre = nullptr) const {
;     ...
;             for (int m = 0; m < 4; ++m) { const int row = EPI_ROWS(ai, m); float rs, gw = 1.f;
;                 if (MOE) { rs = (MOE_FP8 ? opaque_f(1.f / W13_SCALE) : srs[row]); gw = (HAS_PRE ? pre[ai * 4 + m] : sgw[row]) * (MOE_FP8 ? G8_SCALE : 1.f); } else { rs = rstd_q(ssq, row, fq) * ascale; if (f8) gw = G8_SCALE; }
;                 rs8[ai][m] = rs; gw8[ai][m] = gw; }
; #pragma unroll
;         for (int ai = 0; ai < 2; ++ai)
; #pragma unroll
;             for (int m = 0; m < 4; ++m) { const int row = EPI_ROWS(ai, m); const float rs = rs8[ai][m], gw = gw8[ai][m];
;                 const float rs2 = rs * gw; f32x4 o[2];
; #pragma unroll
;                 for (int bj = 0; bj < 2; ++bj)
; #pragma unroll
;                     for (int e = 0; e < 4; ++e) { const float a = acc[ai][bj][m][0][e] * rs, b = acc[ai][bj][m][1][e] * rs2; o[bj][e] = a * fast_sigmoid(a) * b; }
;                 if ((MOE && MOE_FP8) || (!MOE && f8)) { u32x2 w; w.x = pk4_fp8(o[0][0], o[0][1], o[0][2], o[0][3]); w.y = pk4_fp8(o[1][0], o[1][1], o[1][2], o[1][3]);
;                     *(u32x2*)((unsigned char*)G + (size_t)row * DFF + u.pn * HALF + wc * 32 + 8 * fq) = w; }
;                 else *(u32x4*)(G + (size_t)row * DFF + u.pn * HALF + wc * 32 + 8 * fq) = pack8(o[0], o[1]); }
	v_exp_f32_e32 v45, v45
	v_mul_f32_e32 v46, v104, v108
	v_mul_f32_e32 v47, v105, v109
	v_mul_f32_e32 v48, v106, v110
	v_mul_f32_e32 v49, v107, v111
	v_mul_f32_e32 v50, v96, v100
	v_mul_f32_e32 v51, v97, v101
	v_mul_f32_e32 v52, v98, v102
	v_mul_f32_e32 v53, v99, v103
	v_fma_f32 v38, v38, v59, v59
	v_fma_f32 v39, v39, v59, v59
	v_fma_f32 v40, v40, v59, v59
	v_fma_f32 v41, v41, v59, v59
	v_fma_f32 v42, v42, v59, v59
	v_fma_f32 v43, v43, v59, v59
	v_fma_f32 v44, v44, v59, v59
	v_fma_f32 v45, v45, v59, v59
	v_rcp_f32_e32 v38, v38
	v_rcp_f32_e32 v39, v39
	v_rcp_f32_e32 v40, v40
	v_rcp_f32_e32 v41, v41
	v_rcp_f32_e32 v42, v42
	v_rcp_f32_e32 v43, v43
	v_rcp_f32_e32 v44, v44
	v_rcp_f32_e32 v45, v45
	v_mul_f32_e32 v46, v46, v38
	v_mul_f32_e32 v47, v47, v39
	v_mul_f32_e32 v48, v48, v40
	v_mul_f32_e32 v49, v49, v41
	v_mul_f32_e32 v50, v50, v42
	v_mul_f32_e32 v51, v51, v43
	v_mul_f32_e32 v52, v52, v44
	v_mul_f32_e32 v53, v53, v45
	v_med3_f32 v46, v46, s49, v254
	v_med3_f32 v47, v47, s49, v254
	v_med3_f32 v48, v48, s49, v254
	v_med3_f32 v49, v49, s49, v254
	v_med3_f32 v50, v50, s49, v254
	v_med3_f32 v51, v51, s49, v254
	v_med3_f32 v52, v52, s49, v254
	v_med3_f32 v53, v53, s49, v254
	v_cvt_pk_fp8_f32 v34, v46, v47
	v_cvt_pk_fp8_f32 v35, v50, v51
	v_cvt_pk_fp8_f32 v34, v48, v49 op_sel:[0,0,1]
	v_cvt_pk_fp8_f32 v35, v52, v53 op_sel:[0,0,1]
	v_lshl_add_u64 v[8:9], v[4:5], 0, s[20:21]
	global_store_dwordx2 v[8:9], v[34:35], off
	s_mov_b32 s20, 0x8c000
	s_mov_b32 s21, 0
	v_mul_f32_e32 v38, 0xbcb8aa3b, v88
	v_mul_f32_e32 v39, 0xbcb8aa3b, v89
	v_mul_f32_e32 v40, 0xbcb8aa3b, v90
	v_mul_f32_e32 v41, 0xbcb8aa3b, v91
	v_mul_f32_e32 v42, 0xbcb8aa3b, v80
	v_mul_f32_e32 v43, 0xbcb8aa3b, v81
	v_mul_f32_e32 v44, 0xbcb8aa3b, v82
	v_mul_f32_e32 v45, 0xbcb8aa3b, v83
	v_exp_f32_e32 v38, v38
	v_exp_f32_e32 v39, v39
	v_exp_f32_e32 v40, v40
	v_exp_f32_e32 v41, v41
	v_exp_f32_e32 v42, v42
	v_exp_f32_e32 v43, v43
	v_exp_f32_e32 v44, v44
	v_exp_f32_e32 v45, v45
	v_mul_f32_e32 v46, v88, v92
	v_mul_f32_e32 v47, v89, v93
	v_mul_f32_e32 v48, v90, v94
	v_mul_f32_e32 v49, v91, v95
	v_mul_f32_e32 v50, v80, v84
	v_mul_f32_e32 v51, v81, v85
	v_mul_f32_e32 v52, v82, v86
	v_mul_f32_e32 v53, v83, v87
	v_fma_f32 v38, v38, v60, v60
	v_fma_f32 v39, v39, v60, v60
	v_fma_f32 v40, v40, v60, v60
	v_fma_f32 v41, v41, v60, v60
	v_fma_f32 v42, v42, v60, v60
	v_fma_f32 v43, v43, v60, v60
	v_fma_f32 v44, v44, v60, v60
	v_fma_f32 v45, v45, v60, v60
	v_rcp_f32_e32 v38, v38
	v_rcp_f32_e32 v39, v39
	v_rcp_f32_e32 v40, v40
	v_rcp_f32_e32 v41, v41
	v_rcp_f32_e32 v42, v42
	v_rcp_f32_e32 v43, v43
	v_rcp_f32_e32 v44, v44
	v_rcp_f32_e32 v45, v45
	v_mul_f32_e32 v46, v46, v38
	v_mul_f32_e32 v47, v47, v39
	v_mul_f32_e32 v48, v48, v40
	v_mul_f32_e32 v49, v49, v41
	v_mul_f32_e32 v50, v50, v42
	v_mul_f32_e32 v51, v51, v43
	v_mul_f32_e32 v52, v52, v44
	v_mul_f32_e32 v53, v53, v45
	v_med3_f32 v46, v46, s49, v254
	v_med3_f32 v47, v47, s49, v254
	v_med3_f32 v48, v48, s49, v254
	v_med3_f32 v49, v49, s49, v254
	v_med3_f32 v50, v50, s49, v254
	v_med3_f32 v51, v51, s49, v254
	v_med3_f32 v52, v52, s49, v254
	v_med3_f32 v53, v53, s49, v254
	v_cvt_pk_fp8_f32 v32, v46, v47
	v_cvt_pk_fp8_f32 v33, v50, v51
	v_cvt_pk_fp8_f32 v32, v48, v49 op_sel:[0,0,1]
	v_cvt_pk_fp8_f32 v33, v52, v53 op_sel:[0,0,1]
	v_lshl_add_u64 v[8:9], v[4:5], 0, s[20:21]
	global_store_dwordx2 v[8:9], v[32:33], off
	s_mov_b32 s20, 0x9a000
	s_mov_b32 s21, 0
	v_mul_f32_e32 v38, 0xbcb8aa3b, v72
	v_mul_f32_e32 v39, 0xbcb8aa3b, v73
	v_mul_f32_e32 v40, 0xbcb8aa3b, v74
	v_mul_f32_e32 v41, 0xbcb8aa3b, v75
	v_mul_f32_e32 v42, 0xbcb8aa3b, v68
	v_mul_f32_e32 v43, 0xbcb8aa3b, v69
	v_mul_f32_e32 v44, 0xbcb8aa3b, v70
	v_mul_f32_e32 v45, 0xbcb8aa3b, v71
	v_exp_f32_e32 v38, v38
	v_exp_f32_e32 v39, v39
	v_exp_f32_e32 v40, v40
	v_exp_f32_e32 v41, v41
	v_exp_f32_e32 v42, v42
	v_exp_f32_e32 v43, v43
	v_exp_f32_e32 v44, v44
	v_exp_f32_e32 v45, v45
	v_mul_f32_e32 v46, v72, v76
	v_mul_f32_e32 v47, v73, v77
	v_mul_f32_e32 v48, v74, v78
	v_mul_f32_e32 v49, v75, v79
	v_mul_f32_e32 v50, v68, v64
	v_mul_f32_e32 v51, v69, v65
	v_mul_f32_e32 v52, v70, v66
	v_mul_f32_e32 v53, v71, v67
	v_fma_f32 v38, v38, v61, v61
	v_fma_f32 v39, v39, v61, v61
	v_fma_f32 v40, v40, v61, v61
	v_fma_f32 v41, v41, v61, v61
	v_fma_f32 v42, v42, v61, v61
	v_fma_f32 v43, v43, v61, v61
	v_fma_f32 v44, v44, v61, v61
	v_fma_f32 v45, v45, v61, v61
	v_rcp_f32_e32 v38, v38
	v_rcp_f32_e32 v39, v39
	v_rcp_f32_e32 v40, v40
	v_rcp_f32_e32 v41, v41
	v_rcp_f32_e32 v42, v42
	v_rcp_f32_e32 v43, v43
	v_rcp_f32_e32 v44, v44
	v_rcp_f32_e32 v45, v45
	v_mul_f32_e32 v46, v46, v38
	v_mul_f32_e32 v47, v47, v39
	v_mul_f32_e32 v48, v48, v40
	v_mul_f32_e32 v49, v49, v41
	v_mul_f32_e32 v50, v50, v42
	v_mul_f32_e32 v51, v51, v43
	v_mul_f32_e32 v52, v52, v44
	v_mul_f32_e32 v53, v53, v45
	v_med3_f32 v46, v46, s49, v254
	v_med3_f32 v47, v47, s49, v254
	v_med3_f32 v48, v48, s49, v254
	v_med3_f32 v49, v49, s49, v254
	v_med3_f32 v50, v50, s49, v254
	v_med3_f32 v51, v51, s49, v254
	v_med3_f32 v52, v52, s49, v254
	v_med3_f32 v53, v53, s49, v254
	v_cvt_pk_fp8_f32 v34, v46, v47
	v_cvt_pk_fp8_f32 v35, v50, v51
	v_cvt_pk_fp8_f32 v34, v48, v49 op_sel:[0,0,1]
	v_cvt_pk_fp8_f32 v35, v52, v53 op_sel:[0,0,1]
	v_lshl_add_u64 v[8:9], v[4:5], 0, s[20:21]
	global_store_dwordx2 v[8:9], v[34:35], off
	s_mov_b64 s[6:7], -1
	s_cbranch_vccnz .LBB0_1337
	s_andn2_b64 vcc, exec, s[8:9]
	v_mov_b32 v64, 0
	s_cbranch_vccnz .LBB0_1336
	s_barrier
	s_branch .LBB0_1336
